# v38 + P8 prologue (LN2 gain/shift table): the 4 dependent load rounds issued together
# speedup vs baseline: 1.0230x; 1.0021x over previous
.LBB0_1210:
	s_waitcnt lgkmcnt(0)
	v_readfirstlane_b32 s6, v2
	v_readfirstlane_b32 s7, v3
	s_mov_b64 s[8:9], 0x188000
	s_mov_b64 s[10:11], 0x186000
	v_lshl_add_u64 v[8:9], s[50:51], 0, v[4:5]
	v_lshl_add_u64 v[10:11], s[6:7], 0, v[4:5]
	v_lshl_add_u64 v[12:13], v[8:9], 0, s[8:9]
	v_lshl_add_u64 v[8:9], v[8:9], 0, s[10:11]
	global_load_dword v14, v[10:11], off
	global_load_dword v15, v[12:13], off
	global_load_dword v16, v[8:9], off
	v_lshl_add_u64 v[4:5], v[4:5], 0, s[2:3]
	v_lshl_add_u64 v[8:9], s[50:51], 0, v[4:5]
	v_lshl_add_u64 v[10:11], s[6:7], 0, v[4:5]
	v_lshl_add_u64 v[12:13], v[8:9], 0, s[8:9]
	v_lshl_add_u64 v[8:9], v[8:9], 0, s[10:11]
	global_load_dword v17, v[10:11], off
	global_load_dword v18, v[12:13], off
	global_load_dword v19, v[8:9], off
	v_lshl_add_u64 v[4:5], v[4:5], 0, s[2:3]
	v_lshl_add_u64 v[8:9], s[50:51], 0, v[4:5]
	v_lshl_add_u64 v[10:11], s[6:7], 0, v[4:5]
	v_lshl_add_u64 v[12:13], v[8:9], 0, s[8:9]
	v_lshl_add_u64 v[8:9], v[8:9], 0, s[10:11]
	global_load_dword v20, v[10:11], off
	global_load_dword v21, v[12:13], off
	global_load_dword v22, v[8:9], off
	v_lshl_add_u64 v[4:5], v[4:5], 0, s[2:3]
	v_lshl_add_u64 v[8:9], s[50:51], 0, v[4:5]
	v_lshl_add_u64 v[10:11], s[6:7], 0, v[4:5]
	v_lshl_add_u64 v[12:13], v[8:9], 0, s[8:9]
	v_lshl_add_u64 v[8:9], v[8:9], 0, s[10:11]
	global_load_dword v23, v[10:11], off
	global_load_dword v24, v[12:13], off
	global_load_dword v25, v[8:9], off
	v_lshl_add_u64 v[4:5], v[4:5], 0, s[2:3]
	s_waitcnt vmcnt(9)
	v_add_f32_e32 v9, 1.0, v15
	v_mul_f32_e32 v7, v14, v9
	ds_write2st64_b32 v6, v7, v16 offset1:32
	v_add_u32_e32 v6, 0x800, v6
	s_waitcnt vmcnt(6)
	v_add_f32_e32 v9, 1.0, v18
	v_mul_f32_e32 v7, v17, v9
	ds_write2st64_b32 v6, v7, v19 offset1:32
	v_add_u32_e32 v6, 0x800, v6
	s_waitcnt vmcnt(3)
	v_add_f32_e32 v9, 1.0, v21
	v_mul_f32_e32 v7, v20, v9
	ds_write2st64_b32 v6, v7, v22 offset1:32
	v_add_u32_e32 v6, 0x800, v6
	s_waitcnt vmcnt(0)
	v_add_f32_e32 v9, 1.0, v24
	v_mul_f32_e32 v7, v23, v9
	ds_write2st64_b32 v6, v7, v25 offset1:32
	v_add_u32_e32 v6, 0x800, v6
	s_or_b64 exec, exec, s[0:1]
	s_add_i32 s0, 0, 0x27e78
	v_mov_b32_e32 v1, s0
	s_waitcnt lgkmcnt(0)
	s_barrier
	ds_read_b64 v[2:3], v1
	s_cmpk_gt_i32 s90, 0xff
	s_waitcnt lgkmcnt(0)
	v_readfirstlane_b32 s0, v2
	v_readfirstlane_b32 s1, v3
	s_cbranch_scc1 .LBB0_1458
	v_mbcnt_lo_u32_b32 v1, -1, 0
	v_mbcnt_hi_u32_b32 v2, -1, v1
	v_and_b32_e32 v1, 64, v2
	v_add_u32_e32 v3, 64, v1
	v_xor_b32_e32 v1, 1, v2
	v_cmp_lt_i32_e32 vcc, v1, v3
	v_xor_b32_e32 v4, 2, v2
	s_add_u32 s22, s50, 0x700000
	v_cndmask_b32_e32 v1, v2, v1, vcc
	v_cmp_lt_i32_e32 vcc, v4, v3
	s_addc_u32 s23, s51, 0
	s_add_u32 s24, s50, 0x740000
	v_cndmask_b32_e32 v4, v2, v4, vcc
	v_lshlrev_b32_e32 v138, 2, v4
	v_xor_b32_e32 v4, 4, v2
	v_cmp_lt_i32_e32 vcc, v4, v3
	s_addc_u32 s25, s51, 0
	s_add_u32 s26, s50, 0x780000
	v_cndmask_b32_e32 v4, v2, v4, vcc
	v_lshlrev_b32_e32 v139, 2, v4
	v_xor_b32_e32 v4, 8, v2
	s_addc_u32 s27, s51, 0
	v_cmp_lt_i32_e32 vcc, v4, v3
	s_add_u32 s28, s50, 0x8b0000
	s_addc_u32 s29, s51, 0
	v_cndmask_b32_e32 v4, v2, v4, vcc
	v_lshlrev_b32_e32 v140, 2, v4
	v_xor_b32_e32 v4, 16, v2
	s_lshl_b32 s33, s88, 2
	v_cmp_lt_i32_e32 vcc, v4, v3
	s_add_u32 s30, s50, 0x900000
	s_addc_u32 s31, s51, 0
	v_cndmask_b32_e32 v4, v2, v4, vcc
	v_lshlrev_b32_e32 v141, 2, v4
	v_xor_b32_e32 v4, 32, v2
	s_add_u32 s34, s50, 0x940000
	v_cmp_lt_i32_e32 vcc, v4, v3
	s_addc_u32 s35, s51, 0
	v_lshrrev_b32_e32 v3, 6, v0
	v_and_b32_e32 v5, 0xfc, v194
	s_add_i32 s2, 0, 0x20c00
	v_lshl_add_u32 v145, v3, 2, s2
	v_lshl_add_u32 v5, v5, 1, 0
	v_mul_u32_u24_e32 v3, 0x108, v3
	v_lshl_add_u32 v146, v3, 1, v5
	v_or_b32_e32 v3, 0x200, v0
	v_lshrrev_b32_e32 v6, 6, v3
	v_lshl_add_u32 v147, v6, 2, s2
	v_mul_u32_u24_e32 v6, 0x108, v6
	v_lshl_add_u32 v148, v6, 1, v5
	v_or_b32_e32 v6, 0x400, v0
	v_lshrrev_b32_e32 v7, 6, v6
	v_lshl_add_u32 v149, v7, 2, s2
	v_mul_u32_u24_e32 v7, 0x108, v7
	v_lshl_add_u32 v150, v7, 1, v5
	v_or_b32_e32 v7, 0x600, v0
	v_lshrrev_b32_e32 v8, 6, v7
	v_lshl_add_u32 v151, v8, 2, s2
	v_mul_u32_u24_e32 v8, 0x108, v8
	v_lshrrev_b32_e32 v3, 5, v3
	v_lshl_add_u32 v152, v8, 1, v5
	v_lshlrev_b32_e32 v8, 4, v0
	v_mul_u32_u24_e32 v3, 0x108, v3
	v_and_b32_e32 v9, 0x1f0, v8
	s_add_i32 s2, 0, 0x14800
	v_lshlrev_b32_e32 v3, 1, v3
	v_add3_u32 v155, 0, v3, v9
	v_add3_u32 v156, s2, v3, v9
	v_lshrrev_b32_e32 v3, 5, v6
	v_mul_u32_u24_e32 v3, 0x108, v3
	v_lshlrev_b32_e32 v3, 1, v3
	v_lshrrev_b32_e32 v5, 5, v0
	v_add3_u32 v157, 0, v3, v9
	v_add3_u32 v158, s2, v3, v9
	v_lshrrev_b32_e32 v3, 5, v7
	v_mul_u32_u24_e32 v5, 0x108, v5
	v_mul_u32_u24_e32 v3, 0x108, v3
	v_lshlrev_b32_e32 v5, 1, v5
	v_lshlrev_b32_e32 v3, 1, v3
	v_add3_u32 v153, 0, v5, v9
	v_add3_u32 v154, s2, v5, v9
	v_add3_u32 v159, 0, v3, v9
	v_add3_u32 v160, s2, v3, v9
	v_and_b32_e32 v3, 15, v0
	v_and_b32_e32 v5, 48, v0
	v_lshl_or_b32 v5, s88, 6, v5
	v_mul_u32_u24_e32 v6, 0x108, v3
	v_lshlrev_b32_e32 v6, 1, v6
	v_add_u32_e32 v7, s2, v5
	s_add_i32 s2, 0, 0xc400
	v_add3_u32 v161, 0, v5, v6
	v_add3_u32 v162, 0, v6, v5
	v_add_u32_e32 v163, v6, v7
	v_add_u32_e32 v5, s2, v5
	v_add_u32_e32 v9, 0x4200, v6
	v_add_u32_e32 v6, 0x6300, v6
	v_add_u32_e32 v165, v5, v9
	v_add_u32_e32 v167, v5, v6
	s_lshl_b32 s2, s88, 13
	v_lshlrev_b32_e32 v5, 6, v0
	v_add_u32_e32 v166, v7, v9
	v_add_u32_e32 v168, v7, v6
	s_add_i32 s2, s2, 0
	v_and_b32_e32 v7, 0xc00, v5
	v_and_b32_e32 v5, 0x1f00, v8
	v_lshlrev_b32_e32 v130, 4, v3
	v_mov_b32_e32 v131, 0
	v_lshl_add_u32 v6, v3, 2, s2
	v_or_b32_e32 v3, v5, v130
	s_add_i32 s2, 0, 0x1cc00
	v_lshl_add_u64 v[132:133], s[0:1], 0, v[130:131]
	s_add_i32 s0, 0, 0x1ec00
	v_cndmask_b32_e32 v2, v2, v4, vcc
	v_add_u32_e32 v171, s2, v3
	v_add_u32_e32 v172, s0, v3
	v_lshlrev_b32_e32 v3, 8, v0
	v_lshlrev_b32_e32 v142, 2, v2
	v_lshlrev_b32_e32 v2, 2, v196
	v_add_u32_e32 v173, s0, v3
	v_add_u32_e32 v174, s2, v3
	v_mov_b32_e32 v3, v131
	v_lshlrev_b32_e32 v4, 4, v196
	s_add_i32 s38, 0, 0x20c80
	v_add3_u32 v169, 0, v5, v130
	v_mov_b32_e32 v5, v131
	v_lshl_add_u64 v[2:3], s[50:51], 0, v[2:3]
	s_mov_b64 s[0:1], 0x2000000
	v_lshlrev_b32_e32 v1, 2, v1
	v_cmp_eq_u32_e64 s[6:7], 0, v196
	v_add_u32_e32 v143, 0, v4
	v_lshl_add_u32 v144, v0, 2, s38
	s_lshl_b32 s39, s88, 4
	v_add_u32_e32 v164, 0x2100, v163
	v_add_u32_e32 v170, 0xc400, v169
	v_cmp_gt_u32_e64 s[8:9], 32, v0
	v_lshl_add_u64 v[134:135], s[48:49], 0, v[4:5]
	v_lshl_add_u64 v[136:137], v[2:3], 0, s[0:1]
	s_lshl_b32 s40, s90, 18
	s_lshl_b32 s41, s52, 18
	s_movk_i32 s42, 0x1000
	v_mov_b32_e32 v175, 0x358637bd
	s_mov_b32 s43, 0xf800000
	v_mov_b32_e32 v176, 0x260
	s_mov_b32 s44, 0xc3e00000
	s_movk_i32 s45, 0xf000
	v_add_u32_e32 v177, v6, v7
	s_mov_b32 s46, 0xff61b1e6
	v_mov_b32_e32 v178, 1
	s_movk_i32 s47, 0x80
	v_mov_b32_e32 v179, 0x80
	v_mov_b32_e32 v180, 0xff61b1e6
	s_mov_b32 s53, 0x40200000
	v_mov_b32_e32 v181, 0x43e00000
	s_mov_b32 s54, s90
	s_branch .LBB0_1214
